# stack14 plus hand-written E2 epilogue: gate pre-scaled by 64 (exact), column halves exchanged with v_permlane16_swap, 8 global_store_dwordx4 instead of 16 dwordx2 per lane
# speedup vs baseline: 1.0052x; 1.0040x over previous
; DI unsigned pk4_f8(float a, float b, float c, float d) {
;     a = __builtin_amdgcn_fmed3f(a, -448.f, 448.f); b = __builtin_amdgcn_fmed3f(b, -448.f, 448.f); c = __builtin_amdgcn_fmed3f(c, -448.f, 448.f); d = __builtin_amdgcn_fmed3f(d, -448.f, 448.f);
;     int w = __builtin_amdgcn_cvt_pk_fp8_f32(a, b, 0, false); w = __builtin_amdgcn_cvt_pk_fp8_f32(c, d, w, true); return (unsigned)w; }
.LBB4_1544:
	s_lshl_b32 s4, s4, 8
	s_add_i32 s4, s4, s67
	v_mbcnt_lo_u32_b32 v130, -1, 0
	v_mbcnt_hi_u32_b32 v130, -1, v130
	v_and_or_b32 v132, v130, 15, s4
	v_ashrrev_i32_e32 v133, 31, v132
	v_lshl_add_u64 v[156:157], v[132:133], 2, s[12:13]
	global_load_dword v174, v[156:157], off
	global_load_dword v175, v[156:157], off offset:64
	global_load_dword v168, v[156:157], off offset:128
	global_load_dword v169, v[156:157], off offset:192
	global_load_dword v176, v[156:157], off offset:512
	global_load_dword v177, v[156:157], off offset:576
	global_load_dword v155, v[156:157], off offset:640
	global_load_dword v154, v[156:157], off offset:704
	s_lshl_b32 s4, s34, 8
	s_and_b32 s4, s4, 0x700
	s_or_b32 s4, s4, s73
	v_ashrrev_i32_e32 v131, 1, v130
	v_and_b32_e32 v131, -8, v131
	v_bfe_u32 v134, v130, 4, 1
	v_mul_u32_u24_e32 v134, 0x78, v134
	v_add3_u32 v130, s4, v131, v134
	v_ashrrev_i32_e32 v131, 31, v130
	v_lshlrev_b64 v[166:167], 11, v[132:133]
	v_lshl_add_u64 v[172:173], s[14:15], 0, v[166:167]
	v_lshl_add_u64 v[172:173], v[172:173], 0, v[130:131]
	s_mov_b32 s93, 0
	s_waitcnt vmcnt(7)
	v_mul_f32_e32 v174, 0x42800000, v174
	v_mul_f32_e32 v124, v124, v174
	v_mul_f32_e32 v125, v125, v174
	v_mul_f32_e32 v126, v126, v174
	v_mul_f32_e32 v127, v127, v174
	v_mul_f32_e32 v120, v120, v174
	v_mul_f32_e32 v121, v121, v174
	v_mul_f32_e32 v122, v122, v174
	v_mul_f32_e32 v123, v123, v174
	v_mul_f32_e32 v116, v116, v174
	v_mul_f32_e32 v117, v117, v174
	v_mul_f32_e32 v118, v118, v174
	v_mul_f32_e32 v119, v119, v174
	v_mul_f32_e32 v112, v112, v174
	v_mul_f32_e32 v113, v113, v174
	v_mul_f32_e32 v114, v114, v174
	v_mul_f32_e32 v115, v115, v174
	v_med3_f32 v124, v124, s87, v153
	v_med3_f32 v125, v125, s87, v153
	v_med3_f32 v126, v126, s87, v153
	v_med3_f32 v127, v127, s87, v153
	v_med3_f32 v120, v120, s87, v153
	v_med3_f32 v121, v121, s87, v153
	v_med3_f32 v122, v122, s87, v153
	v_med3_f32 v123, v123, s87, v153
	v_med3_f32 v116, v116, s87, v153
	v_med3_f32 v117, v117, s87, v153
	v_med3_f32 v118, v118, s87, v153
	v_med3_f32 v119, v119, s87, v153
	v_med3_f32 v112, v112, s87, v153
	v_med3_f32 v113, v113, s87, v153
	v_med3_f32 v114, v114, s87, v153
	v_med3_f32 v115, v115, s87, v153
	v_cvt_pk_fp8_f32 v180, v124, v125
	v_cvt_pk_fp8_f32 v180, v126, v127 op_sel:[0,0,1]
	v_cvt_pk_fp8_f32 v181, v120, v121
	v_cvt_pk_fp8_f32 v181, v122, v123 op_sel:[0,0,1]
	v_cvt_pk_fp8_f32 v182, v116, v117
	v_cvt_pk_fp8_f32 v182, v118, v119 op_sel:[0,0,1]
	v_cvt_pk_fp8_f32 v183, v112, v113
	v_cvt_pk_fp8_f32 v183, v114, v115 op_sel:[0,0,1]
	s_nop 1
	v_permlane16_swap_b32_e32 v180, v182
	v_permlane16_swap_b32_e32 v181, v183
	global_store_dwordx4 v[172:173], v[180:183], off
	s_waitcnt vmcnt(7)
	v_mul_f32_e32 v175, 0x42800000, v175
	v_mul_f32_e32 v108, v108, v175
	v_mul_f32_e32 v109, v109, v175
	v_mul_f32_e32 v110, v110, v175
	v_mul_f32_e32 v111, v111, v175
	v_mul_f32_e32 v104, v104, v175
	v_mul_f32_e32 v105, v105, v175
	v_mul_f32_e32 v106, v106, v175
	v_mul_f32_e32 v107, v107, v175
	v_mul_f32_e32 v100, v100, v175
	v_mul_f32_e32 v101, v101, v175
	v_mul_f32_e32 v102, v102, v175
	v_mul_f32_e32 v103, v103, v175
	v_mul_f32_e32 v96, v96, v175
	v_mul_f32_e32 v97, v97, v175
	v_mul_f32_e32 v98, v98, v175
	v_mul_f32_e32 v99, v99, v175
	v_med3_f32 v108, v108, s87, v153
	v_med3_f32 v109, v109, s87, v153
	v_med3_f32 v110, v110, s87, v153
	v_med3_f32 v111, v111, s87, v153
	v_med3_f32 v104, v104, s87, v153
	v_med3_f32 v105, v105, s87, v153
	v_med3_f32 v106, v106, s87, v153
	v_med3_f32 v107, v107, s87, v153
	v_med3_f32 v100, v100, s87, v153
	v_med3_f32 v101, v101, s87, v153
	v_med3_f32 v102, v102, s87, v153
	v_med3_f32 v103, v103, s87, v153
	v_med3_f32 v96, v96, s87, v153
	v_med3_f32 v97, v97, s87, v153
	v_med3_f32 v98, v98, s87, v153
	v_med3_f32 v99, v99, s87, v153
	v_cvt_pk_fp8_f32 v184, v108, v109
	v_cvt_pk_fp8_f32 v184, v110, v111 op_sel:[0,0,1]
	v_cvt_pk_fp8_f32 v185, v104, v105
	v_cvt_pk_fp8_f32 v185, v106, v107 op_sel:[0,0,1]
	v_cvt_pk_fp8_f32 v186, v100, v101
	v_cvt_pk_fp8_f32 v186, v102, v103 op_sel:[0,0,1]
	v_cvt_pk_fp8_f32 v187, v96, v97
	v_cvt_pk_fp8_f32 v187, v98, v99 op_sel:[0,0,1]
	s_mov_b32 s92, 0x8000
	v_lshl_add_u64 v[138:139], v[172:173], 0, s[92:93]
	v_permlane16_swap_b32_e32 v184, v186
	v_permlane16_swap_b32_e32 v185, v187
	global_store_dwordx4 v[138:139], v[184:187], off
	s_waitcnt vmcnt(7)
	v_mul_f32_e32 v168, 0x42800000, v168
	v_mul_f32_e32 v92, v92, v168
	v_mul_f32_e32 v93, v93, v168
	v_mul_f32_e32 v94, v94, v168
	v_mul_f32_e32 v95, v95, v168
	v_mul_f32_e32 v88, v88, v168
	v_mul_f32_e32 v89, v89, v168
	v_mul_f32_e32 v90, v90, v168
	v_mul_f32_e32 v91, v91, v168
	v_mul_f32_e32 v84, v84, v168
	v_mul_f32_e32 v85, v85, v168
	v_mul_f32_e32 v86, v86, v168
	v_mul_f32_e32 v87, v87, v168
	v_mul_f32_e32 v80, v80, v168
	v_mul_f32_e32 v81, v81, v168
	v_mul_f32_e32 v82, v82, v168
	v_mul_f32_e32 v83, v83, v168
	v_med3_f32 v92, v92, s87, v153
	v_med3_f32 v93, v93, s87, v153
	v_med3_f32 v94, v94, s87, v153
	v_med3_f32 v95, v95, s87, v153
	v_med3_f32 v88, v88, s87, v153
	v_med3_f32 v89, v89, s87, v153
	v_med3_f32 v90, v90, s87, v153
	v_med3_f32 v91, v91, s87, v153
	v_med3_f32 v84, v84, s87, v153
	v_med3_f32 v85, v85, s87, v153
	v_med3_f32 v86, v86, s87, v153
	v_med3_f32 v87, v87, s87, v153
	v_med3_f32 v80, v80, s87, v153
	v_med3_f32 v81, v81, s87, v153
	v_med3_f32 v82, v82, s87, v153
	v_med3_f32 v83, v83, s87, v153
	v_cvt_pk_fp8_f32 v180, v92, v93
	v_cvt_pk_fp8_f32 v180, v94, v95 op_sel:[0,0,1]
	v_cvt_pk_fp8_f32 v181, v88, v89
	v_cvt_pk_fp8_f32 v181, v90, v91 op_sel:[0,0,1]
	v_cvt_pk_fp8_f32 v182, v84, v85
	v_cvt_pk_fp8_f32 v182, v86, v87 op_sel:[0,0,1]
	v_cvt_pk_fp8_f32 v183, v80, v81
	v_cvt_pk_fp8_f32 v183, v82, v83 op_sel:[0,0,1]
	s_mov_b32 s92, 0x10000
	v_lshl_add_u64 v[136:137], v[172:173], 0, s[92:93]
	v_permlane16_swap_b32_e32 v180, v182
	v_permlane16_swap_b32_e32 v181, v183
	global_store_dwordx4 v[136:137], v[180:183], off
	s_waitcnt vmcnt(7)
; DI unsigned pk4_f8(float a, float b, float c, float d) {
;     a = __builtin_amdgcn_fmed3f(a, -448.f, 448.f); b = __builtin_amdgcn_fmed3f(b, -448.f, 448.f); c = __builtin_amdgcn_fmed3f(c, -448.f, 448.f); d = __builtin_amdgcn_fmed3f(d, -448.f, 448.f);
;     int w = __builtin_amdgcn_cvt_pk_fp8_f32(a, b, 0, false); w = __builtin_amdgcn_cvt_pk_fp8_f32(c, d, w, true); return (unsigned)w; }
	v_mul_f32_e32 v169, 0x42800000, v169
	v_mul_f32_e32 v76, v76, v169
	v_mul_f32_e32 v77, v77, v169
	v_mul_f32_e32 v78, v78, v169
	v_mul_f32_e32 v79, v79, v169
	v_mul_f32_e32 v72, v72, v169
	v_mul_f32_e32 v73, v73, v169
	v_mul_f32_e32 v74, v74, v169
	v_mul_f32_e32 v75, v75, v169
	v_mul_f32_e32 v68, v68, v169
	v_mul_f32_e32 v69, v69, v169
	v_mul_f32_e32 v70, v70, v169
	v_mul_f32_e32 v71, v71, v169
	v_mul_f32_e32 v64, v64, v169
	v_mul_f32_e32 v65, v65, v169
	v_mul_f32_e32 v66, v66, v169
	v_mul_f32_e32 v67, v67, v169
	v_med3_f32 v76, v76, s87, v153
	v_med3_f32 v77, v77, s87, v153
	v_med3_f32 v78, v78, s87, v153
	v_med3_f32 v79, v79, s87, v153
	v_med3_f32 v72, v72, s87, v153
	v_med3_f32 v73, v73, s87, v153
	v_med3_f32 v74, v74, s87, v153
	v_med3_f32 v75, v75, s87, v153
	v_med3_f32 v68, v68, s87, v153
	v_med3_f32 v69, v69, s87, v153
	v_med3_f32 v70, v70, s87, v153
	v_med3_f32 v71, v71, s87, v153
	v_med3_f32 v64, v64, s87, v153
	v_med3_f32 v65, v65, s87, v153
	v_med3_f32 v66, v66, s87, v153
	v_med3_f32 v67, v67, s87, v153
	v_cvt_pk_fp8_f32 v184, v76, v77
	v_cvt_pk_fp8_f32 v184, v78, v79 op_sel:[0,0,1]
	v_cvt_pk_fp8_f32 v185, v72, v73
	v_cvt_pk_fp8_f32 v185, v74, v75 op_sel:[0,0,1]
	v_cvt_pk_fp8_f32 v186, v68, v69
	v_cvt_pk_fp8_f32 v186, v70, v71 op_sel:[0,0,1]
	v_cvt_pk_fp8_f32 v187, v64, v65
	v_cvt_pk_fp8_f32 v187, v66, v67 op_sel:[0,0,1]
	s_mov_b32 s92, 0x18000
	v_lshl_add_u64 v[138:139], v[172:173], 0, s[92:93]
	v_permlane16_swap_b32_e32 v184, v186
	v_permlane16_swap_b32_e32 v185, v187
	global_store_dwordx4 v[138:139], v[184:187], off
	s_waitcnt vmcnt(7)
	v_mul_f32_e32 v176, 0x42800000, v176
	v_mul_f32_e32 v60, v60, v176
	v_mul_f32_e32 v61, v61, v176
	v_mul_f32_e32 v62, v62, v176
	v_mul_f32_e32 v63, v63, v176
	v_mul_f32_e32 v56, v56, v176
	v_mul_f32_e32 v57, v57, v176
	v_mul_f32_e32 v58, v58, v176
	v_mul_f32_e32 v59, v59, v176
	v_mul_f32_e32 v52, v52, v176
	v_mul_f32_e32 v53, v53, v176
	v_mul_f32_e32 v54, v54, v176
	v_mul_f32_e32 v55, v55, v176
	v_mul_f32_e32 v48, v48, v176
	v_mul_f32_e32 v49, v49, v176
	v_mul_f32_e32 v50, v50, v176
	v_mul_f32_e32 v51, v51, v176
	v_med3_f32 v60, v60, s87, v153
	v_med3_f32 v61, v61, s87, v153
	v_med3_f32 v62, v62, s87, v153
	v_med3_f32 v63, v63, s87, v153
	v_med3_f32 v56, v56, s87, v153
	v_med3_f32 v57, v57, s87, v153
	v_med3_f32 v58, v58, s87, v153
	v_med3_f32 v59, v59, s87, v153
	v_med3_f32 v52, v52, s87, v153
	v_med3_f32 v53, v53, s87, v153
	v_med3_f32 v54, v54, s87, v153
	v_med3_f32 v55, v55, s87, v153
	v_med3_f32 v48, v48, s87, v153
	v_med3_f32 v49, v49, s87, v153
	v_med3_f32 v50, v50, s87, v153
	v_med3_f32 v51, v51, s87, v153
	v_cvt_pk_fp8_f32 v180, v60, v61
	v_cvt_pk_fp8_f32 v180, v62, v63 op_sel:[0,0,1]
	v_cvt_pk_fp8_f32 v181, v56, v57
	v_cvt_pk_fp8_f32 v181, v58, v59 op_sel:[0,0,1]
	v_cvt_pk_fp8_f32 v182, v52, v53
	v_cvt_pk_fp8_f32 v182, v54, v55 op_sel:[0,0,1]
	v_cvt_pk_fp8_f32 v183, v48, v49
	v_cvt_pk_fp8_f32 v183, v50, v51 op_sel:[0,0,1]
	s_mov_b32 s92, 0x40000
	v_lshl_add_u64 v[136:137], v[172:173], 0, s[92:93]
	v_permlane16_swap_b32_e32 v180, v182
	v_permlane16_swap_b32_e32 v181, v183
	global_store_dwordx4 v[136:137], v[180:183], off
	s_waitcnt vmcnt(7)
	v_mul_f32_e32 v177, 0x42800000, v177
	v_mul_f32_e32 v44, v44, v177
	v_mul_f32_e32 v45, v45, v177
	v_mul_f32_e32 v46, v46, v177
	v_mul_f32_e32 v47, v47, v177
	v_mul_f32_e32 v40, v40, v177
	v_mul_f32_e32 v41, v41, v177
	v_mul_f32_e32 v42, v42, v177
	v_mul_f32_e32 v43, v43, v177
	v_mul_f32_e32 v36, v36, v177
	v_mul_f32_e32 v37, v37, v177
	v_mul_f32_e32 v38, v38, v177
	v_mul_f32_e32 v39, v39, v177
	v_mul_f32_e32 v32, v32, v177
	v_mul_f32_e32 v33, v33, v177
	v_mul_f32_e32 v34, v34, v177
	v_mul_f32_e32 v35, v35, v177
	v_med3_f32 v44, v44, s87, v153
	v_med3_f32 v45, v45, s87, v153
	v_med3_f32 v46, v46, s87, v153
	v_med3_f32 v47, v47, s87, v153
	v_med3_f32 v40, v40, s87, v153
	v_med3_f32 v41, v41, s87, v153
	v_med3_f32 v42, v42, s87, v153
	v_med3_f32 v43, v43, s87, v153
	v_med3_f32 v36, v36, s87, v153
	v_med3_f32 v37, v37, s87, v153
	v_med3_f32 v38, v38, s87, v153
	v_med3_f32 v39, v39, s87, v153
	v_med3_f32 v32, v32, s87, v153
	v_med3_f32 v33, v33, s87, v153
	v_med3_f32 v34, v34, s87, v153
	v_med3_f32 v35, v35, s87, v153
	v_cvt_pk_fp8_f32 v184, v44, v45
	v_cvt_pk_fp8_f32 v184, v46, v47 op_sel:[0,0,1]
	v_cvt_pk_fp8_f32 v185, v40, v41
	v_cvt_pk_fp8_f32 v185, v42, v43 op_sel:[0,0,1]
	v_cvt_pk_fp8_f32 v186, v36, v37
	v_cvt_pk_fp8_f32 v186, v38, v39 op_sel:[0,0,1]
	v_cvt_pk_fp8_f32 v187, v32, v33
	v_cvt_pk_fp8_f32 v187, v34, v35 op_sel:[0,0,1]
	s_mov_b32 s92, 0x48000
	v_lshl_add_u64 v[138:139], v[172:173], 0, s[92:93]
	v_permlane16_swap_b32_e32 v184, v186
	v_permlane16_swap_b32_e32 v185, v187
	global_store_dwordx4 v[138:139], v[184:187], off
	s_waitcnt vmcnt(7)
; #define PG8_BAR __builtin_amdgcn_s_barrier()
;     ...
;         if (!has_next) break;
; #pragma unroll
;         for (int a = 0; a < 2; ++a)
; #pragma unroll
;             for (int b = 0; b < 2; ++b)
; #pragma unroll
;                 for (int m = 0; m < 4; ++m)
; #pragma unroll
;                     for (int n = 0; n < 2; ++n) acc[a][b][m][n] = (f32x4){0.f, 0.f, 0.f, 0.f};
;         cur = nxt; cA = nA; cB = nB; ++ui;
;         if constexpr (ALIGN_EPI) { if (wr == 1) PG8_BAR; }
	v_mul_f32_e32 v155, 0x42800000, v155
	v_mul_f32_e32 v28, v28, v155
	v_mul_f32_e32 v29, v29, v155
	v_mul_f32_e32 v30, v30, v155
	v_mul_f32_e32 v31, v31, v155
	v_mul_f32_e32 v24, v24, v155
	v_mul_f32_e32 v25, v25, v155
	v_mul_f32_e32 v26, v26, v155
	v_mul_f32_e32 v27, v27, v155
	v_mul_f32_e32 v20, v20, v155
	v_mul_f32_e32 v21, v21, v155
	v_mul_f32_e32 v22, v22, v155
	v_mul_f32_e32 v23, v23, v155
	v_mul_f32_e32 v16, v16, v155
	v_mul_f32_e32 v17, v17, v155
	v_mul_f32_e32 v18, v18, v155
	v_mul_f32_e32 v19, v19, v155
	v_med3_f32 v28, v28, s87, v153
	v_med3_f32 v29, v29, s87, v153
	v_med3_f32 v30, v30, s87, v153
	v_med3_f32 v31, v31, s87, v153
	v_med3_f32 v24, v24, s87, v153
	v_med3_f32 v25, v25, s87, v153
	v_med3_f32 v26, v26, s87, v153
	v_med3_f32 v27, v27, s87, v153
	v_med3_f32 v20, v20, s87, v153
	v_med3_f32 v21, v21, s87, v153
	v_med3_f32 v22, v22, s87, v153
	v_med3_f32 v23, v23, s87, v153
	v_med3_f32 v16, v16, s87, v153
	v_med3_f32 v17, v17, s87, v153
	v_med3_f32 v18, v18, s87, v153
	v_med3_f32 v19, v19, s87, v153
	v_cvt_pk_fp8_f32 v180, v28, v29
	v_cvt_pk_fp8_f32 v180, v30, v31 op_sel:[0,0,1]
	v_cvt_pk_fp8_f32 v181, v24, v25
	v_cvt_pk_fp8_f32 v181, v26, v27 op_sel:[0,0,1]
	v_cvt_pk_fp8_f32 v182, v20, v21
	v_cvt_pk_fp8_f32 v182, v22, v23 op_sel:[0,0,1]
	v_cvt_pk_fp8_f32 v183, v16, v17
	v_cvt_pk_fp8_f32 v183, v18, v19 op_sel:[0,0,1]
	s_mov_b32 s92, 0x50000
	v_lshl_add_u64 v[136:137], v[172:173], 0, s[92:93]
	v_permlane16_swap_b32_e32 v180, v182
	v_permlane16_swap_b32_e32 v181, v183
	global_store_dwordx4 v[136:137], v[180:183], off
	s_waitcnt vmcnt(7)
	v_mul_f32_e32 v154, 0x42800000, v154
	v_mul_f32_e32 v12, v12, v154
	v_mul_f32_e32 v13, v13, v154
	v_mul_f32_e32 v14, v14, v154
	v_mul_f32_e32 v15, v15, v154
	v_mul_f32_e32 v8, v8, v154
	v_mul_f32_e32 v9, v9, v154
	v_mul_f32_e32 v10, v10, v154
	v_mul_f32_e32 v11, v11, v154
	v_mul_f32_e32 v4, v4, v154
	v_mul_f32_e32 v5, v5, v154
	v_mul_f32_e32 v6, v6, v154
	v_mul_f32_e32 v7, v7, v154
	v_mul_f32_e32 v0, v0, v154
	v_mul_f32_e32 v1, v1, v154
	v_mul_f32_e32 v2, v2, v154
	v_mul_f32_e32 v3, v3, v154
	v_med3_f32 v12, v12, s87, v153
	v_med3_f32 v13, v13, s87, v153
	v_med3_f32 v14, v14, s87, v153
	v_med3_f32 v15, v15, s87, v153
	v_med3_f32 v8, v8, s87, v153
	v_med3_f32 v9, v9, s87, v153
	v_med3_f32 v10, v10, s87, v153
	v_med3_f32 v11, v11, s87, v153
	v_med3_f32 v4, v4, s87, v153
	v_med3_f32 v5, v5, s87, v153
	v_med3_f32 v6, v6, s87, v153
	v_med3_f32 v7, v7, s87, v153
	v_med3_f32 v0, v0, s87, v153
	v_med3_f32 v1, v1, s87, v153
	v_med3_f32 v2, v2, s87, v153
	v_med3_f32 v3, v3, s87, v153
	v_cvt_pk_fp8_f32 v184, v12, v13
	v_cvt_pk_fp8_f32 v184, v14, v15 op_sel:[0,0,1]
	v_cvt_pk_fp8_f32 v185, v8, v9
	v_cvt_pk_fp8_f32 v185, v10, v11 op_sel:[0,0,1]
	v_cvt_pk_fp8_f32 v186, v4, v5
	v_cvt_pk_fp8_f32 v186, v6, v7 op_sel:[0,0,1]
	v_cvt_pk_fp8_f32 v187, v0, v1
	v_cvt_pk_fp8_f32 v187, v2, v3 op_sel:[0,0,1]
	s_mov_b32 s92, 0x58000
	v_lshl_add_u64 v[138:139], v[172:173], 0, s[92:93]
	v_permlane16_swap_b32_e32 v184, v186
	v_permlane16_swap_b32_e32 v185, v187
	global_store_dwordx4 v[138:139], v[184:187], off
	s_andn2_b64 vcc, exec, s[26:27]
	s_mov_b64 s[26:27], -1
	s_cbranch_vccnz .LBB4_1532
	s_andn2_b64 vcc, exec, s[8:9]
	s_cbranch_vccnz .LBB4_1531
	s_barrier
	s_branch .LBB4_1531
